# K1 loop fully unrolled and double-buffered: next 8KB of loads issued before the current 8KB is reduced (16KB in flight per wave)
# speedup vs baseline: 1.0846x; 1.0138x over previous
.LBB0_8:
	v_mov_b32_e32 v46, v68
	buffer_load_dwordx4 v[26:29], v46, s[8:11], 0 offen sc0 nt
	buffer_load_dwordx4 v[34:37], v46, s[8:11], 0 offen offset:2048 sc0 nt
	buffer_load_dwordx4 v[10:13], v46, s[8:11], 0 offen offset:1024 sc0 nt
	buffer_load_dwordx4 v[14:17], v46, s[8:11], 0 offen offset:3072 sc0 nt
	v_add_u32_e32 v47, 0x1000, v46
	buffer_load_dwordx4 v[30:33], v47, s[8:11], 0 offen sc0 nt
	buffer_load_dwordx4 v[38:41], v47, s[8:11], 0 offen offset:2048 sc0 nt
	buffer_load_dwordx4 v[18:21], v47, s[8:11], 0 offen offset:1024 sc0 nt
	buffer_load_dwordx4 v[22:25], v47, s[8:11], 0 offen offset:3072 sc0 nt
	v_add_u32_e32 v46, 0x8000, v68
	buffer_load_dwordx4 v[96:99], v46, s[8:11], 0 offen sc0 nt
	buffer_load_dwordx4 v[104:107], v46, s[8:11], 0 offen offset:2048 sc0 nt
	buffer_load_dwordx4 v[80:83], v46, s[8:11], 0 offen offset:1024 sc0 nt
	buffer_load_dwordx4 v[84:87], v46, s[8:11], 0 offen offset:3072 sc0 nt
	v_add_u32_e32 v47, 0x1000, v46
	buffer_load_dwordx4 v[100:103], v47, s[8:11], 0 offen sc0 nt
	buffer_load_dwordx4 v[108:111], v47, s[8:11], 0 offen offset:2048 sc0 nt
	buffer_load_dwordx4 v[88:91], v47, s[8:11], 0 offen offset:1024 sc0 nt
	buffer_load_dwordx4 v[92:95], v47, s[8:11], 0 offen offset:3072 sc0 nt
	s_bitcmp1_b32 s15, 8
	s_cselect_b64 s[20:21], -1, 0
	s_lshr_b32 s16, s15, 2
	s_and_b32 s16, s16, 63
	s_lshl_b64 s[4:5], 1, s16
	s_waitcnt vmcnt(12)
	v_pk_add_f32 v[72:73], v[26:27], v[28:29]
	v_pk_add_f32 v[74:75], v[10:11], v[12:13]
	v_pk_add_f32 v[76:77], v[34:35], v[36:37]
	v_pk_add_f32 v[78:79], v[14:15], v[16:17]
	v_pk_add_f32 v[58:59], v[26:27], v[34:35]
	v_pk_add_f32 v[60:61], v[28:29], v[36:37]
	v_pk_add_f32 v[72:73], v[72:73], v[74:75]
	v_pk_add_f32 v[76:77], v[76:77], v[78:79]
	v_pk_add_f32 v[54:55], v[10:11], v[14:15]
	v_pk_add_f32 v[56:57], v[12:13], v[16:17]
	v_add_f32_e32 v50, v72, v73
	v_add_f32_e32 v51, v76, v77
	s_waitcnt vmcnt(8)
	v_pk_add_f32 v[72:73], v[30:31], v[32:33]
	v_pk_add_f32 v[74:75], v[18:19], v[20:21]
	v_pk_add_f32 v[76:77], v[38:39], v[40:41]
	v_pk_add_f32 v[78:79], v[22:23], v[24:25]
	v_pk_add_f32 v[48:49], v[30:31], v[38:39]
	v_pk_add_f32 v[70:71], v[32:33], v[40:41]
	v_pk_add_f32 v[72:73], v[72:73], v[74:75]
	v_pk_add_f32 v[76:77], v[76:77], v[78:79]
	v_pk_add_f32 v[58:59], v[58:59], v[48:49]
	v_pk_add_f32 v[60:61], v[60:61], v[70:71]
	v_pk_add_f32 v[48:49], v[18:19], v[22:23]
	v_pk_add_f32 v[70:71], v[20:21], v[24:25]
	v_add_f32_e32 v52, v72, v73
	v_add_f32_e32 v53, v76, v77
	v_pk_add_f32 v[2:3], v[2:3], v[58:59]
	v_pk_add_f32 v[4:5], v[4:5], v[60:61]
	v_pk_add_f32 v[54:55], v[54:55], v[48:49]
	v_pk_add_f32 v[56:57], v[56:57], v[70:71]
	v_add_f32_e32 v72, v50, v51
	v_add_f32_e32 v73, v52, v53
	v_pk_add_f32 v[6:7], v[6:7], v[54:55]
	v_pk_add_f32 v[8:9], v[8:9], v[56:57]
	v_add_f32_e32 v72, v72, v73
	v_add_f32_e32 v43, v43, v72
	v_add_f32_dpp v50, v50, v50 quad_perm:[1,0,3,2] row_mask:0xf bank_mask:0xf
	v_add_f32_dpp v51, v51, v51 quad_perm:[1,0,3,2] row_mask:0xf bank_mask:0xf
	v_add_f32_dpp v52, v52, v52 quad_perm:[1,0,3,2] row_mask:0xf bank_mask:0xf
	v_add_f32_dpp v53, v53, v53 quad_perm:[1,0,3,2] row_mask:0xf bank_mask:0xf
	v_add_f32_dpp v50, v50, v50 quad_perm:[2,3,0,1] row_mask:0xf bank_mask:0xf
	v_add_f32_dpp v51, v51, v51 quad_perm:[2,3,0,1] row_mask:0xf bank_mask:0xf
	v_add_f32_dpp v52, v52, v52 quad_perm:[2,3,0,1] row_mask:0xf bank_mask:0xf
	v_add_f32_dpp v53, v53, v53 quad_perm:[2,3,0,1] row_mask:0xf bank_mask:0xf
	v_add_f32_dpp v50, v50, v50 row_half_mirror row_mask:0xf bank_mask:0xf
	v_add_f32_dpp v51, v51, v51 row_half_mirror row_mask:0xf bank_mask:0xf
	v_add_f32_dpp v52, v52, v52 row_half_mirror row_mask:0xf bank_mask:0xf
	v_add_f32_dpp v53, v53, v53 row_half_mirror row_mask:0xf bank_mask:0xf
	v_add_f32_dpp v50, v50, v50 row_mirror row_mask:0xf bank_mask:0xf
	v_add_f32_dpp v51, v51, v51 row_mirror row_mask:0xf bank_mask:0xf
	v_add_f32_dpp v52, v52, v52 row_mirror row_mask:0xf bank_mask:0xf
	v_add_f32_dpp v53, v53, v53 row_mirror row_mask:0xf bank_mask:0xf
	v_add_f32_dpp v50, v50, v50 row_bcast:15 row_mask:0xa bank_mask:0xf
	v_add_f32_dpp v51, v51, v51 row_bcast:15 row_mask:0xa bank_mask:0xf
	v_add_f32_dpp v52, v52, v52 row_bcast:15 row_mask:0xa bank_mask:0xf
	v_add_f32_dpp v53, v53, v53 row_bcast:15 row_mask:0xa bank_mask:0xf
	v_add_f32_dpp v50, v50, v50 row_bcast:31 row_mask:0xc bank_mask:0xf
	v_add_f32_dpp v51, v51, v51 row_bcast:31 row_mask:0xc bank_mask:0xf
	v_add_f32_dpp v52, v52, v52 row_bcast:31 row_mask:0xc bank_mask:0xf
	v_add_f32_dpp v53, v53, v53 row_bcast:31 row_mask:0xc bank_mask:0xf
	s_mov_b64 exec, s[4:5]
	v_cndmask_b32_e64 v58, v26, v10, s[20:21]
	v_cndmask_b32_e64 v59, v35, v15, s[20:21]
	v_cndmask_b32_e64 v60, v32, v20, s[20:21]
	v_cndmask_b32_e64 v61, v41, v25, s[20:21]
	global_store_dwordx4 v[44:45], v[58:61], off
	v_add_f32_e32 v72, v58, v59
	v_add_f32_e32 v73, v60, v61
	v_add_f32_e32 v72, v72, v73
	v_add_f32_e32 v42, v42, v72
	s_mov_b32 s4, 0
	s_brev_b32 s5, 1
	s_mov_b64 exec, s[4:5]
	v_lshl_add_u64 v[72:73], v[44:45], 0, s[18:19]
	global_store_dwordx4 v[72:73], v[50:53], off
	s_mov_b64 exec, -1
	s_add_u32 s15, s15, 16
	v_lshl_add_u64 v[44:45], v[44:45], 0, 64
	v_add_u32_e32 v46, 0x10000, v68
	buffer_load_dwordx4 v[26:29], v46, s[8:11], 0 offen sc0 nt
	buffer_load_dwordx4 v[34:37], v46, s[8:11], 0 offen offset:2048 sc0 nt
	buffer_load_dwordx4 v[10:13], v46, s[8:11], 0 offen offset:1024 sc0 nt
	buffer_load_dwordx4 v[14:17], v46, s[8:11], 0 offen offset:3072 sc0 nt
	v_add_u32_e32 v47, 0x1000, v46
	buffer_load_dwordx4 v[30:33], v47, s[8:11], 0 offen sc0 nt
	buffer_load_dwordx4 v[38:41], v47, s[8:11], 0 offen offset:2048 sc0 nt
	buffer_load_dwordx4 v[18:21], v47, s[8:11], 0 offen offset:1024 sc0 nt
	buffer_load_dwordx4 v[22:25], v47, s[8:11], 0 offen offset:3072 sc0 nt
	s_bitcmp1_b32 s15, 8
	s_cselect_b64 s[20:21], -1, 0
	s_lshr_b32 s16, s15, 2
	s_and_b32 s16, s16, 63
	s_lshl_b64 s[4:5], 1, s16
	s_waitcnt vmcnt(14)
	v_pk_add_f32 v[72:73], v[96:97], v[98:99]
	v_pk_add_f32 v[74:75], v[80:81], v[82:83]
	v_pk_add_f32 v[76:77], v[104:105], v[106:107]
	v_pk_add_f32 v[78:79], v[84:85], v[86:87]
	v_pk_add_f32 v[58:59], v[96:97], v[104:105]
	v_pk_add_f32 v[60:61], v[98:99], v[106:107]
	v_pk_add_f32 v[72:73], v[72:73], v[74:75]
	v_pk_add_f32 v[76:77], v[76:77], v[78:79]
	v_pk_add_f32 v[54:55], v[80:81], v[84:85]
	v_pk_add_f32 v[56:57], v[82:83], v[86:87]
	v_add_f32_e32 v50, v72, v73
	v_add_f32_e32 v51, v76, v77
	s_waitcnt vmcnt(10)
	v_pk_add_f32 v[72:73], v[100:101], v[102:103]
	v_pk_add_f32 v[74:75], v[88:89], v[90:91]
	v_pk_add_f32 v[76:77], v[108:109], v[110:111]
	v_pk_add_f32 v[78:79], v[92:93], v[94:95]
	v_pk_add_f32 v[48:49], v[100:101], v[108:109]
	v_pk_add_f32 v[70:71], v[102:103], v[110:111]
	v_pk_add_f32 v[72:73], v[72:73], v[74:75]
	v_pk_add_f32 v[76:77], v[76:77], v[78:79]
	v_pk_add_f32 v[58:59], v[58:59], v[48:49]
	v_pk_add_f32 v[60:61], v[60:61], v[70:71]
	v_pk_add_f32 v[48:49], v[88:89], v[92:93]
	v_pk_add_f32 v[70:71], v[90:91], v[94:95]
	v_add_f32_e32 v52, v72, v73
	v_add_f32_e32 v53, v76, v77
	v_pk_add_f32 v[2:3], v[2:3], v[58:59]
	v_pk_add_f32 v[4:5], v[4:5], v[60:61]
	v_pk_add_f32 v[54:55], v[54:55], v[48:49]
	v_pk_add_f32 v[56:57], v[56:57], v[70:71]
	v_add_f32_e32 v72, v50, v51
	v_add_f32_e32 v73, v52, v53
	v_pk_add_f32 v[6:7], v[6:7], v[54:55]
	v_pk_add_f32 v[8:9], v[8:9], v[56:57]
	v_add_f32_e32 v72, v72, v73
	v_add_f32_e32 v43, v43, v72
	v_add_f32_dpp v50, v50, v50 quad_perm:[1,0,3,2] row_mask:0xf bank_mask:0xf
	v_add_f32_dpp v51, v51, v51 quad_perm:[1,0,3,2] row_mask:0xf bank_mask:0xf
	v_add_f32_dpp v52, v52, v52 quad_perm:[1,0,3,2] row_mask:0xf bank_mask:0xf
	v_add_f32_dpp v53, v53, v53 quad_perm:[1,0,3,2] row_mask:0xf bank_mask:0xf
	v_add_f32_dpp v50, v50, v50 quad_perm:[2,3,0,1] row_mask:0xf bank_mask:0xf
	v_add_f32_dpp v51, v51, v51 quad_perm:[2,3,0,1] row_mask:0xf bank_mask:0xf
	v_add_f32_dpp v52, v52, v52 quad_perm:[2,3,0,1] row_mask:0xf bank_mask:0xf
	v_add_f32_dpp v53, v53, v53 quad_perm:[2,3,0,1] row_mask:0xf bank_mask:0xf
	v_add_f32_dpp v50, v50, v50 row_half_mirror row_mask:0xf bank_mask:0xf
	v_add_f32_dpp v51, v51, v51 row_half_mirror row_mask:0xf bank_mask:0xf
	v_add_f32_dpp v52, v52, v52 row_half_mirror row_mask:0xf bank_mask:0xf
	v_add_f32_dpp v53, v53, v53 row_half_mirror row_mask:0xf bank_mask:0xf
	v_add_f32_dpp v50, v50, v50 row_mirror row_mask:0xf bank_mask:0xf
	v_add_f32_dpp v51, v51, v51 row_mirror row_mask:0xf bank_mask:0xf
	v_add_f32_dpp v52, v52, v52 row_mirror row_mask:0xf bank_mask:0xf
	v_add_f32_dpp v53, v53, v53 row_mirror row_mask:0xf bank_mask:0xf
	v_add_f32_dpp v50, v50, v50 row_bcast:15 row_mask:0xa bank_mask:0xf
	v_add_f32_dpp v51, v51, v51 row_bcast:15 row_mask:0xa bank_mask:0xf
	v_add_f32_dpp v52, v52, v52 row_bcast:15 row_mask:0xa bank_mask:0xf
	v_add_f32_dpp v53, v53, v53 row_bcast:15 row_mask:0xa bank_mask:0xf
	v_add_f32_dpp v50, v50, v50 row_bcast:31 row_mask:0xc bank_mask:0xf
	v_add_f32_dpp v51, v51, v51 row_bcast:31 row_mask:0xc bank_mask:0xf
	v_add_f32_dpp v52, v52, v52 row_bcast:31 row_mask:0xc bank_mask:0xf
	v_add_f32_dpp v53, v53, v53 row_bcast:31 row_mask:0xc bank_mask:0xf
	s_mov_b64 exec, s[4:5]
	v_cndmask_b32_e64 v58, v96, v80, s[20:21]
	v_cndmask_b32_e64 v59, v105, v85, s[20:21]
	v_cndmask_b32_e64 v60, v102, v90, s[20:21]
	v_cndmask_b32_e64 v61, v111, v95, s[20:21]
	global_store_dwordx4 v[44:45], v[58:61], off
	v_add_f32_e32 v72, v58, v59
	v_add_f32_e32 v73, v60, v61
	v_add_f32_e32 v72, v72, v73
	v_add_f32_e32 v42, v42, v72
	s_mov_b32 s4, 0
	s_brev_b32 s5, 1
	s_mov_b64 exec, s[4:5]
	v_lshl_add_u64 v[72:73], v[44:45], 0, s[18:19]
	global_store_dwordx4 v[72:73], v[50:53], off
	s_mov_b64 exec, -1
	s_add_u32 s15, s15, 16
	v_lshl_add_u64 v[44:45], v[44:45], 0, 64
	v_add_u32_e32 v46, 0x18000, v68
	buffer_load_dwordx4 v[96:99], v46, s[8:11], 0 offen sc0 nt
	buffer_load_dwordx4 v[104:107], v46, s[8:11], 0 offen offset:2048 sc0 nt
	buffer_load_dwordx4 v[80:83], v46, s[8:11], 0 offen offset:1024 sc0 nt
	buffer_load_dwordx4 v[84:87], v46, s[8:11], 0 offen offset:3072 sc0 nt
	v_add_u32_e32 v47, 0x1000, v46
	buffer_load_dwordx4 v[100:103], v47, s[8:11], 0 offen sc0 nt
	buffer_load_dwordx4 v[108:111], v47, s[8:11], 0 offen offset:2048 sc0 nt
	buffer_load_dwordx4 v[88:91], v47, s[8:11], 0 offen offset:1024 sc0 nt
	buffer_load_dwordx4 v[92:95], v47, s[8:11], 0 offen offset:3072 sc0 nt
	s_bitcmp1_b32 s15, 8
	s_cselect_b64 s[20:21], -1, 0
	s_lshr_b32 s16, s15, 2
	s_and_b32 s16, s16, 63
	s_lshl_b64 s[4:5], 1, s16
	s_waitcnt vmcnt(14)
	v_pk_add_f32 v[72:73], v[26:27], v[28:29]
	v_pk_add_f32 v[74:75], v[10:11], v[12:13]
	v_pk_add_f32 v[76:77], v[34:35], v[36:37]
	v_pk_add_f32 v[78:79], v[14:15], v[16:17]
	v_pk_add_f32 v[58:59], v[26:27], v[34:35]
	v_pk_add_f32 v[60:61], v[28:29], v[36:37]
	v_pk_add_f32 v[72:73], v[72:73], v[74:75]
	v_pk_add_f32 v[76:77], v[76:77], v[78:79]
	v_pk_add_f32 v[54:55], v[10:11], v[14:15]
	v_pk_add_f32 v[56:57], v[12:13], v[16:17]
	v_add_f32_e32 v50, v72, v73
	v_add_f32_e32 v51, v76, v77
	s_waitcnt vmcnt(10)
	v_pk_add_f32 v[72:73], v[30:31], v[32:33]
	v_pk_add_f32 v[74:75], v[18:19], v[20:21]
	v_pk_add_f32 v[76:77], v[38:39], v[40:41]
	v_pk_add_f32 v[78:79], v[22:23], v[24:25]
	v_pk_add_f32 v[48:49], v[30:31], v[38:39]
	v_pk_add_f32 v[70:71], v[32:33], v[40:41]
	v_pk_add_f32 v[72:73], v[72:73], v[74:75]
	v_pk_add_f32 v[76:77], v[76:77], v[78:79]
	v_pk_add_f32 v[58:59], v[58:59], v[48:49]
	v_pk_add_f32 v[60:61], v[60:61], v[70:71]
	v_pk_add_f32 v[48:49], v[18:19], v[22:23]
	v_pk_add_f32 v[70:71], v[20:21], v[24:25]
	v_add_f32_e32 v52, v72, v73
	v_add_f32_e32 v53, v76, v77
	v_pk_add_f32 v[2:3], v[2:3], v[58:59]
	v_pk_add_f32 v[4:5], v[4:5], v[60:61]
	v_pk_add_f32 v[54:55], v[54:55], v[48:49]
	v_pk_add_f32 v[56:57], v[56:57], v[70:71]
	v_add_f32_e32 v72, v50, v51
	v_add_f32_e32 v73, v52, v53
	v_pk_add_f32 v[6:7], v[6:7], v[54:55]
	v_pk_add_f32 v[8:9], v[8:9], v[56:57]
	v_add_f32_e32 v72, v72, v73
	v_add_f32_e32 v43, v43, v72
	v_add_f32_dpp v50, v50, v50 quad_perm:[1,0,3,2] row_mask:0xf bank_mask:0xf
	v_add_f32_dpp v51, v51, v51 quad_perm:[1,0,3,2] row_mask:0xf bank_mask:0xf
	v_add_f32_dpp v52, v52, v52 quad_perm:[1,0,3,2] row_mask:0xf bank_mask:0xf
	v_add_f32_dpp v53, v53, v53 quad_perm:[1,0,3,2] row_mask:0xf bank_mask:0xf
	v_add_f32_dpp v50, v50, v50 quad_perm:[2,3,0,1] row_mask:0xf bank_mask:0xf
	v_add_f32_dpp v51, v51, v51 quad_perm:[2,3,0,1] row_mask:0xf bank_mask:0xf
	v_add_f32_dpp v52, v52, v52 quad_perm:[2,3,0,1] row_mask:0xf bank_mask:0xf
	v_add_f32_dpp v53, v53, v53 quad_perm:[2,3,0,1] row_mask:0xf bank_mask:0xf
	v_add_f32_dpp v50, v50, v50 row_half_mirror row_mask:0xf bank_mask:0xf
	v_add_f32_dpp v51, v51, v51 row_half_mirror row_mask:0xf bank_mask:0xf
	v_add_f32_dpp v52, v52, v52 row_half_mirror row_mask:0xf bank_mask:0xf
	v_add_f32_dpp v53, v53, v53 row_half_mirror row_mask:0xf bank_mask:0xf
	v_add_f32_dpp v50, v50, v50 row_mirror row_mask:0xf bank_mask:0xf
	v_add_f32_dpp v51, v51, v51 row_mirror row_mask:0xf bank_mask:0xf
	v_add_f32_dpp v52, v52, v52 row_mirror row_mask:0xf bank_mask:0xf
	v_add_f32_dpp v53, v53, v53 row_mirror row_mask:0xf bank_mask:0xf
	v_add_f32_dpp v50, v50, v50 row_bcast:15 row_mask:0xa bank_mask:0xf
	v_add_f32_dpp v51, v51, v51 row_bcast:15 row_mask:0xa bank_mask:0xf
	v_add_f32_dpp v52, v52, v52 row_bcast:15 row_mask:0xa bank_mask:0xf
	v_add_f32_dpp v53, v53, v53 row_bcast:15 row_mask:0xa bank_mask:0xf
	v_add_f32_dpp v50, v50, v50 row_bcast:31 row_mask:0xc bank_mask:0xf
	v_add_f32_dpp v51, v51, v51 row_bcast:31 row_mask:0xc bank_mask:0xf
	v_add_f32_dpp v52, v52, v52 row_bcast:31 row_mask:0xc bank_mask:0xf
	v_add_f32_dpp v53, v53, v53 row_bcast:31 row_mask:0xc bank_mask:0xf
	s_mov_b64 exec, s[4:5]
	v_cndmask_b32_e64 v58, v26, v10, s[20:21]
	v_cndmask_b32_e64 v59, v35, v15, s[20:21]
	v_cndmask_b32_e64 v60, v32, v20, s[20:21]
	v_cndmask_b32_e64 v61, v41, v25, s[20:21]
	global_store_dwordx4 v[44:45], v[58:61], off
	v_add_f32_e32 v72, v58, v59
	v_add_f32_e32 v73, v60, v61
	v_add_f32_e32 v72, v72, v73
	v_add_f32_e32 v42, v42, v72
	s_mov_b32 s4, 0
	s_brev_b32 s5, 1
	s_mov_b64 exec, s[4:5]
	v_lshl_add_u64 v[72:73], v[44:45], 0, s[18:19]
	global_store_dwordx4 v[72:73], v[50:53], off
	s_mov_b64 exec, -1
	s_add_u32 s15, s15, 16
	v_lshl_add_u64 v[44:45], v[44:45], 0, 64
	s_bitcmp1_b32 s15, 8
	s_cselect_b64 s[20:21], -1, 0
	s_lshr_b32 s16, s15, 2
	s_and_b32 s16, s16, 63
	s_lshl_b64 s[4:5], 1, s16
	s_waitcnt vmcnt(6)
	v_pk_add_f32 v[72:73], v[96:97], v[98:99]
	v_pk_add_f32 v[74:75], v[80:81], v[82:83]
	v_pk_add_f32 v[76:77], v[104:105], v[106:107]
	v_pk_add_f32 v[78:79], v[84:85], v[86:87]
	v_pk_add_f32 v[58:59], v[96:97], v[104:105]
	v_pk_add_f32 v[60:61], v[98:99], v[106:107]
	v_pk_add_f32 v[72:73], v[72:73], v[74:75]
	v_pk_add_f32 v[76:77], v[76:77], v[78:79]
	v_pk_add_f32 v[54:55], v[80:81], v[84:85]
	v_pk_add_f32 v[56:57], v[82:83], v[86:87]
	v_add_f32_e32 v50, v72, v73
	v_add_f32_e32 v51, v76, v77
	s_waitcnt vmcnt(2)
	v_pk_add_f32 v[72:73], v[100:101], v[102:103]
	v_pk_add_f32 v[74:75], v[88:89], v[90:91]
	v_pk_add_f32 v[76:77], v[108:109], v[110:111]
	v_pk_add_f32 v[78:79], v[92:93], v[94:95]
	v_pk_add_f32 v[48:49], v[100:101], v[108:109]
	v_pk_add_f32 v[70:71], v[102:103], v[110:111]
	v_pk_add_f32 v[72:73], v[72:73], v[74:75]
	v_pk_add_f32 v[76:77], v[76:77], v[78:79]
	v_pk_add_f32 v[58:59], v[58:59], v[48:49]
	v_pk_add_f32 v[60:61], v[60:61], v[70:71]
	v_pk_add_f32 v[48:49], v[88:89], v[92:93]
	v_pk_add_f32 v[70:71], v[90:91], v[94:95]
	v_add_f32_e32 v52, v72, v73
	v_add_f32_e32 v53, v76, v77
	v_pk_add_f32 v[2:3], v[2:3], v[58:59]
	v_pk_add_f32 v[4:5], v[4:5], v[60:61]
	v_pk_add_f32 v[54:55], v[54:55], v[48:49]
	v_pk_add_f32 v[56:57], v[56:57], v[70:71]
	v_add_f32_e32 v72, v50, v51
	v_add_f32_e32 v73, v52, v53
	v_pk_add_f32 v[6:7], v[6:7], v[54:55]
	v_pk_add_f32 v[8:9], v[8:9], v[56:57]
	v_add_f32_e32 v72, v72, v73
	v_add_f32_e32 v43, v43, v72
	v_add_f32_dpp v50, v50, v50 quad_perm:[1,0,3,2] row_mask:0xf bank_mask:0xf
	v_add_f32_dpp v51, v51, v51 quad_perm:[1,0,3,2] row_mask:0xf bank_mask:0xf
	v_add_f32_dpp v52, v52, v52 quad_perm:[1,0,3,2] row_mask:0xf bank_mask:0xf
	v_add_f32_dpp v53, v53, v53 quad_perm:[1,0,3,2] row_mask:0xf bank_mask:0xf
	v_add_f32_dpp v50, v50, v50 quad_perm:[2,3,0,1] row_mask:0xf bank_mask:0xf
	v_add_f32_dpp v51, v51, v51 quad_perm:[2,3,0,1] row_mask:0xf bank_mask:0xf
	v_add_f32_dpp v52, v52, v52 quad_perm:[2,3,0,1] row_mask:0xf bank_mask:0xf
	v_add_f32_dpp v53, v53, v53 quad_perm:[2,3,0,1] row_mask:0xf bank_mask:0xf
	v_add_f32_dpp v50, v50, v50 row_half_mirror row_mask:0xf bank_mask:0xf
	v_add_f32_dpp v51, v51, v51 row_half_mirror row_mask:0xf bank_mask:0xf
	v_add_f32_dpp v52, v52, v52 row_half_mirror row_mask:0xf bank_mask:0xf
	v_add_f32_dpp v53, v53, v53 row_half_mirror row_mask:0xf bank_mask:0xf
	v_add_f32_dpp v50, v50, v50 row_mirror row_mask:0xf bank_mask:0xf
	v_add_f32_dpp v51, v51, v51 row_mirror row_mask:0xf bank_mask:0xf
	v_add_f32_dpp v52, v52, v52 row_mirror row_mask:0xf bank_mask:0xf
	v_add_f32_dpp v53, v53, v53 row_mirror row_mask:0xf bank_mask:0xf
	v_add_f32_dpp v50, v50, v50 row_bcast:15 row_mask:0xa bank_mask:0xf
	v_add_f32_dpp v51, v51, v51 row_bcast:15 row_mask:0xa bank_mask:0xf
	v_add_f32_dpp v52, v52, v52 row_bcast:15 row_mask:0xa bank_mask:0xf
	v_add_f32_dpp v53, v53, v53 row_bcast:15 row_mask:0xa bank_mask:0xf
	v_add_f32_dpp v50, v50, v50 row_bcast:31 row_mask:0xc bank_mask:0xf
	v_add_f32_dpp v51, v51, v51 row_bcast:31 row_mask:0xc bank_mask:0xf
	v_add_f32_dpp v52, v52, v52 row_bcast:31 row_mask:0xc bank_mask:0xf
	v_add_f32_dpp v53, v53, v53 row_bcast:31 row_mask:0xc bank_mask:0xf
	s_mov_b64 exec, s[4:5]
	v_cndmask_b32_e64 v58, v96, v80, s[20:21]
	v_cndmask_b32_e64 v59, v105, v85, s[20:21]
	v_cndmask_b32_e64 v60, v102, v90, s[20:21]
	v_cndmask_b32_e64 v61, v111, v95, s[20:21]
	global_store_dwordx4 v[44:45], v[58:61], off
	v_add_f32_e32 v72, v58, v59
	v_add_f32_e32 v73, v60, v61
	v_add_f32_e32 v72, v72, v73
	v_add_f32_e32 v42, v42, v72
	s_mov_b32 s4, 0
	s_brev_b32 s5, 1
	s_mov_b64 exec, s[4:5]
	v_lshl_add_u64 v[72:73], v[44:45], 0, s[18:19]
	global_store_dwordx4 v[72:73], v[50:53], off
	s_mov_b64 exec, -1
	s_add_u32 s15, s15, 16
	v_lshl_add_u64 v[44:45], v[44:45], 0, 64

	.amdhsa_kernel _Z9k1_streamPKfPf6PfArgs
		.amdhsa_group_segment_fixed_size 8224
		.amdhsa_private_segment_fixed_size 0
		.amdhsa_kernarg_size 80
		.amdhsa_user_sgpr_count 2
		.amdhsa_user_sgpr_dispatch_ptr 0
		.amdhsa_user_sgpr_queue_ptr 0
		.amdhsa_user_sgpr_kernarg_segment_ptr 1
		.amdhsa_user_sgpr_dispatch_id 0
		.amdhsa_user_sgpr_kernarg_preload_length 0
		.amdhsa_user_sgpr_kernarg_preload_offset 0
		.amdhsa_user_sgpr_private_segment_size 0
		.amdhsa_uses_dynamic_stack 0
		.amdhsa_enable_private_segment 0
		.amdhsa_system_sgpr_workgroup_id_x 1
		.amdhsa_system_sgpr_workgroup_id_y 0
		.amdhsa_system_sgpr_workgroup_id_z 0
		.amdhsa_system_sgpr_workgroup_info 0
		.amdhsa_system_vgpr_workitem_id 0
		.amdhsa_next_free_vgpr 112
		.amdhsa_next_free_sgpr 22
		.amdhsa_accum_offset 112
		.amdhsa_reserve_vcc 1
		.amdhsa_float_round_mode_32 0
		.amdhsa_float_round_mode_16_64 0
		.amdhsa_float_denorm_mode_32 3
		.amdhsa_float_denorm_mode_16_64 3
		.amdhsa_dx10_clamp 1
		.amdhsa_ieee_mode 1
		.amdhsa_fp16_overflow 0
		.amdhsa_tg_split 0
		.amdhsa_exception_fp_ieee_invalid_op 0
		.amdhsa_exception_fp_denorm_src 0
		.amdhsa_exception_fp_ieee_div_zero 0
		.amdhsa_exception_fp_ieee_overflow 0
		.amdhsa_exception_fp_ieee_underflow 0
		.amdhsa_exception_fp_ieee_inexact 0
		.amdhsa_exception_int_div_zero 0
	.end_amdhsa_kernel

amdhsa.kernels:
  - .agpr_count:     0
    .args:
      - .actual_access:  read_only
        .address_space:  global
        .offset:         0
        .size:           8
        .value_kind:     global_buffer
      - .actual_access:  write_only
        .address_space:  global
        .offset:         8
        .size:           8
        .value_kind:     global_buffer
      - .offset:         16
        .size:           64
        .value_kind:     by_value
    .group_segment_fixed_size: 8224
    .kernarg_segment_align: 8
    .kernarg_segment_size: 80
    .language:       OpenCL C
    .language_version:
      - 2
      - 0
    .max_flat_workgroup_size: 256
    .name:           _Z9k1_streamPKfPf6PfArgs
    .private_segment_fixed_size: 0
    .sgpr_count:     28
    .sgpr_spill_count: 0
    .symbol:         _Z9k1_streamPKfPf6PfArgs.kd
    .uniform_work_group_size: 1
    .uses_dynamic_stack: false
    .vgpr_count:     112
    .vgpr_spill_count: 0
    .wavefront_size: 64
  - .agpr_count:     0
    .args:
      - .actual_access:  read_only
        .address_space:  global
        .offset:         0
        .size:           8
        .value_kind:     global_buffer
      - .actual_access:  read_only
        .address_space:  global
        .offset:         8
        .size:           8
        .value_kind:     global_buffer
      - .actual_access:  read_only
        .address_space:  global
        .offset:         16
        .size:           8
        .value_kind:     global_buffer
      - .actual_access:  write_only
        .address_space:  global
        .offset:         24
        .size:           8
        .value_kind:     global_buffer
      - .address_space:  global
        .offset:         32
        .size:           8
        .value_kind:     global_buffer
      - .address_space:  global
        .offset:         40
        .size:           8
        .value_kind:     global_buffer
    .group_segment_fixed_size: 3712
    .kernarg_segment_align: 8
    .kernarg_segment_size: 48
    .language:       OpenCL C
    .language_version:
      - 2
      - 0
    .max_flat_workgroup_size: 256
    .name:           _Z9k2_layer1PKfS0_S0_PfS1_S1_
    .private_segment_fixed_size: 0
    .sgpr_count:     32
    .sgpr_spill_count: 0
    .symbol:         _Z9k2_layer1PKfS0_S0_PfS1_S1_.kd
    .uniform_work_group_size: 1
    .uses_dynamic_stack: false
    .vgpr_count:     92
    .vgpr_spill_count: 0
    .wavefront_size: 64
  - .agpr_count:     8
    .args:
      - .actual_access:  read_only
        .address_space:  global
        .offset:         0
        .size:           8
        .value_kind:     global_buffer
      - .actual_access:  read_only
        .address_space:  global
        .offset:         8
        .size:           8
        .value_kind:     global_buffer
      - .actual_access:  read_only
        .address_space:  global
        .offset:         16
        .size:           8
        .value_kind:     global_buffer
      - .actual_access:  read_only
        .address_space:  global
        .offset:         24
        .size:           8
        .value_kind:     global_buffer
      - .actual_access:  read_only
        .address_space:  global
        .offset:         32
        .size:           8
        .value_kind:     global_buffer
      - .actual_access:  read_only
        .address_space:  global
        .offset:         40
        .size:           8
        .value_kind:     global_buffer
      - .actual_access:  read_only
        .address_space:  global
        .offset:         48
        .size:           8
        .value_kind:     global_buffer
      - .actual_access:  write_only
        .address_space:  global
        .offset:         56
        .size:           8
        .value_kind:     global_buffer
      - .address_space:  global
        .offset:         64
        .size:           8
        .value_kind:     global_buffer
      - .address_space:  global
        .offset:         72
        .size:           8
        .value_kind:     global_buffer
    .group_segment_fixed_size: 1280
    .kernarg_segment_align: 8
    .kernarg_segment_size: 80
    .language:       OpenCL C
    .language_version:
      - 2
      - 0
    .max_flat_workgroup_size: 256
    .name:           _Z7k_layerPKfS0_S0_S0_S0_S0_S0_PfS1_S1_
    .private_segment_fixed_size: 0
    .sgpr_count:     40
    .sgpr_spill_count: 0
    .symbol:         _Z7k_layerPKfS0_S0_S0_S0_S0_S0_PfS1_S1_.kd
    .uniform_work_group_size: 1
    .uses_dynamic_stack: false
    .vgpr_count:     104
    .vgpr_spill_count: 0
    .wavefront_size: 64
  - .agpr_count:     12
    .args:
      - .actual_access:  read_only
        .address_space:  global
        .offset:         0
        .size:           8
        .value_kind:     global_buffer
      - .actual_access:  read_only
        .address_space:  global
        .offset:         8
        .size:           8
        .value_kind:     global_buffer
      - .actual_access:  read_only
        .address_space:  global
        .offset:         16
        .size:           8
        .value_kind:     global_buffer
      - .actual_access:  read_only
        .address_space:  global
        .offset:         24
        .size:           8
        .value_kind:     global_buffer
      - .actual_access:  read_only
        .address_space:  global
        .offset:         32
        .size:           8
        .value_kind:     global_buffer
      - .actual_access:  read_only
        .address_space:  global
        .offset:         40
        .size:           8
        .value_kind:     global_buffer
      - .actual_access:  read_only
        .address_space:  global
        .offset:         48
        .size:           8
        .value_kind:     global_buffer
      - .actual_access:  read_only
        .address_space:  global
        .offset:         56
        .size:           8
        .value_kind:     global_buffer
      - .actual_access:  read_only
        .address_space:  global
        .offset:         64
        .size:           8
        .value_kind:     global_buffer
      - .actual_access:  write_only
        .address_space:  global
        .offset:         72
        .size:           8
        .value_kind:     global_buffer
    .group_segment_fixed_size: 4608
    .kernarg_segment_align: 8
    .kernarg_segment_size: 80
    .language:       OpenCL C
    .language_version:
      - 2
      - 0
    .max_flat_workgroup_size: 256
    .name:           _Z8k5_finalPKfS0_S0_S0_S0_S0_S0_S0_S0_Pf
    .private_segment_fixed_size: 0
    .sgpr_count:     30
    .sgpr_spill_count: 0
    .symbol:         _Z8k5_finalPKfS0_S0_S0_S0_S0_S0_S0_S0_Pf.kd
    .uniform_work_group_size: 1
    .uses_dynamic_stack: false
    .vgpr_count:     96
    .vgpr_spill_count: 0
    .wavefront_size: 64
